# v65 + every hot-loop head 8-byte aligned (padding off the hot paths)
# baseline (speedup 1.0000x reference)
.LBB0_812:
	s_or_b64 exec, exec, s[6:7]
	s_lshl_b32 s6, s16, 8
	s_mul_i32 s8, s30, 0x900
	s_ashr_i32 s7, s6, 31
	s_mul_hi_i32 s3, s30, 0x900
	s_add_u32 s78, s8, s6
	s_addc_u32 s79, s3, s7
	s_mul_i32 s6, s78, s69
	s_mul_hi_u32 s7, s78, s68
	s_add_i32 s6, s7, s6
	s_mul_i32 s7, s79, s68
	s_add_i32 s7, s6, s7
	s_mul_i32 s6, s78, s68
	s_lshl_b64 s[6:7], s[6:7], 1
	s_add_u32 s9, s60, s6
	s_mul_i32 s6, s15, s26
	s_addc_u32 s11, s61, s7
	s_ashr_i32 s7, s6, 31
	s_lshl_b64 s[6:7], s[6:7], 1
	s_add_u32 s10, s9, s6
	s_mul_i32 s3, s3, s62
	s_mul_hi_u32 s6, s8, s62
	s_addc_u32 s11, s11, s7
	s_add_i32 s7, s6, s3
	s_mul_i32 s6, s8, s62
	s_lshl_b64 s[8:9], s[6:7], 1
	s_add_u32 s3, s66, s8
	s_addc_u32 s22, s67, s9
	s_abs_i32 s7, s15
	s_mul_hi_u32 s20, s7, s13
	s_mul_i32 s21, s20, s89
	s_sub_i32 s7, s7, s21
	s_ashr_i32 s6, s15, 31
	s_add_i32 s21, s20, 1
	s_sub_i32 s23, s7, s89
	s_cmp_ge_u32 s7, s89
	s_cselect_b32 s20, s21, s20
	v_ashrrev_i32_e32 v20, 4, v8
	v_and_b32_e32 v3, 0xfffff0, v20
	v_lshlrev_b32_e32 v4, 1, v20
	s_cselect_b32 s7, s23, s7
	s_add_i32 s21, s20, 1
	v_lshlrev_b32_e32 v1, 3, v8
	v_and_or_b32 v3, v4, 8, v3
	s_cmp_ge_u32 s7, s89
	v_and_b32_e32 v2, 0x78, v1
	v_lshrrev_b32_e32 v3, 1, v3
	v_bfe_u32 v1, v1, 5, 2
	s_cselect_b32 s7, s21, s20
	v_or_b32_e32 v3, v3, v1
	s_xor_b32 s7, s7, s6
	v_lshrrev_b32_e32 v4, 1, v20
	v_lshlrev_b32_e32 v21, 9, v3
	v_and_b32_e32 v3, 3, v20
	s_sub_i32 s6, s7, s6
	v_and_or_b32 v3, v4, 4, v3
	v_add_u32_e32 v24, 32, v20
	s_mul_i32 s6, s6, s27
	v_lshlrev_b32_e32 v22, 6, v3
	v_and_b32_e32 v3, 0xfffff0, v24
	v_lshlrev_b32_e32 v4, 1, v24
	s_ashr_i32 s7, s6, 31
	v_and_or_b32 v3, v4, 8, v3
	s_lshl_b64 s[20:21], s[6:7], 1
	v_lshrrev_b32_e32 v3, 1, v3
	s_add_u32 s6, s3, s20
	v_or_b32_e32 v1, v3, v1
	s_addc_u32 s7, s22, s21
	v_lshlrev_b32_e32 v25, 9, v1
	v_mul_lo_u32 v1, v20, s62
	s_add_u32 s3, s85, s8
	v_or_b32_e32 v3, v1, v2
	v_add_u32_e32 v1, s14, v1
	s_addc_u32 s9, s81, s9
	v_and_b32_e32 v0, 63, v8
	v_or_b32_e32 v1, v1, v2
	v_lshlrev_b32_e32 v26, 4, v8
	s_add_u32 s8, s3, s20
	v_lshlrev_b32_e32 v23, 1, v2
	v_lshlrev_b32_e32 v178, 1, v1
	v_lshlrev_b32_e32 v0, 3, v0
	v_and_b32_e32 v1, 0xc0, v26
	v_lshlrev_b32_e32 v2, 1, v8
	s_addc_u32 s9, s9, s21
	v_lshlrev_b32_e32 v128, 1, v3
	v_and_or_b32 v1, v0, 24, v1
	v_and_b32_e32 v2, 32, v2
	v_and_b32_e32 v0, 0x100, v0
	v_or3_b32 v181, v1, v2, v0
	global_load_dwordx4 v[10:13], v128, s[8:9]
	global_load_dwordx4 v[14:17], v178, s[8:9]
	global_load_dwordx4 v[4:7], v128, s[6:7]
	global_load_dwordx4 v[0:3], v178, s[6:7]
	v_ashrrev_i32_e32 v27, 1, v8
	v_bfi_b32 v18, s84, v27, v8
	v_ashrrev_i32_e32 v19, 31, v27
	v_mul_lo_u32 v28, s68, v19
	v_mul_lo_u32 v29, s69, v18
	v_mad_u64_u32 v[18:19], s[20:21], s68, v18, 0
	v_bfe_u32 v182, v8, 5, 1
	v_add3_u32 v19, v19, v28, v29
	v_lshl_add_u64 v[18:19], v[18:19], 1, s[10:11]
	v_lshlrev_b32_e32 v32, 4, v182
	v_mov_b32_e32 v33, v129
	v_lshl_add_u64 v[18:19], v[18:19], 0, v[32:33]
	global_load_dwordx4 v[120:123], v[18:19], off
	global_load_dwordx4 v[124:127], v[18:19], off offset:32
	global_load_dwordx4 v[116:119], v[18:19], off offset:64
	global_load_dwordx4 v[112:115], v[18:19], off offset:96
	global_load_dwordx4 v[108:111], v[18:19], off offset:128
	global_load_dwordx4 v[104:107], v[18:19], off offset:160
	global_load_dwordx4 v[100:103], v[18:19], off offset:192
	global_load_dwordx4 v[96:99], v[18:19], off offset:224
	v_and_b32_e32 v18, 48, v23
	v_or3_b32 v19, v21, v22, v18
	v_add_u32_e32 v201, 0, v19
	v_lshrrev_b32_e32 v19, 3, v201
	v_xor_b32_e32 v19, v19, v201
	v_and_b32_e32 v19, 0x100, v19
	v_xor_b32_e32 v201, v201, v19
	v_lshlrev_b32_e32 v19, 3, v19
	v_xor_b32_e32 v201, v201, v19
	v_and_b32_e32 v9, 31, v8
	v_ashrrev_i32_e32 v21, 7, v8
	s_waitcnt vmcnt(0)
	v_and_b32_e32 v8, 0x70, v8
	v_or3_b32 v18, v25, v22, v18
	v_add_u32_e32 v202, 0, v18
	v_lshrrev_b32_e32 v18, 3, v202
	v_xor_b32_e32 v18, v18, v202
	v_and_b32_e32 v18, 0x100, v18
	v_xor_b32_e32 v202, v202, v18
	v_lshlrev_b32_e32 v18, 3, v18
	v_xor_b32_e32 v202, v202, v18
	v_lshlrev_b32_e32 v33, 8, v9
	v_and_b32_e32 v42, 0x70, v26
	v_add_u32_e32 v184, s2, v21
	v_max_i32_e32 v21, 4, v184
	v_add_u32_e32 v21, -4, v21
	v_min_u32_e32 v185, 24, v21
	v_and_or_b32 v183, v27, 32, v9
	v_or_b32_e32 v34, 32, v32
	v_bitop3_b32 v34, v34, v33, v42 bitop3:0xde
	v_add_u32_e32 v200, 0, v34
	s_cmp_lg_u32 0, -1
	s_cselect_b32 s3, 0, 0
	v_add_u32_e32 v186, s3, v181
	v_add_u32_e32 v188, 7, v185
	ds_write_b128 v201, v[10:13]
	v_lshlrev_b32_e32 v10, 8, v20
	v_bitop3_b32 v10, v23, v10, v8 bitop3:0xde
	v_add_u32_e32 v203, 0, v10
	ds_write_b128 v202, v[14:17]
	ds_write_b128 v203, v[4:7] offset:32768
	v_lshlrev_b32_e32 v4, 8, v24
	v_bitop3_b32 v4, v23, v4, v8 bitop3:0xde
	v_add_u32_e32 v204, 0, v4
	ds_write_b128 v204, v[0:3] offset:32768
	v_bitop3_b32 v0, v32, v33, v42 bitop3:0xde
	v_add_u32_e32 v198, 0, v0
	s_waitcnt lgkmcnt(0)
	s_barrier
	ds_read_b128 v[0:3], v198 offset:32768
	ds_read_b128 v[4:7], v198 offset:40960
	s_waitcnt vmcnt(7) lgkmcnt(1)
	v_mfma_f32_32x32x16_bf16 v[16:31], v[0:3], v[120:123], 0
	ds_read_b128 v[34:37], v200 offset:32768
	ds_read_b128 v[38:41], v200 offset:40960
	s_waitcnt lgkmcnt(2)
	v_mfma_f32_32x32x16_bf16 v[0:15], v[4:7], v[120:123], 0
	s_waitcnt vmcnt(6) lgkmcnt(1)
	v_mfma_f32_32x32x16_bf16 v[16:31], v[34:37], v[124:127], v[16:31]
	v_or_b32_e32 v34, 64, v32
	v_bitop3_b32 v34, v34, v33, v42 bitop3:0xde
	v_add_u32_e32 v199, 0, v34
	s_waitcnt lgkmcnt(0)
	v_mfma_f32_32x32x16_bf16 v[0:15], v[38:41], v[124:127], v[0:15]
	ds_read_b128 v[34:37], v199 offset:32768
	ds_read_b128 v[38:41], v199 offset:40960
	s_waitcnt vmcnt(5) lgkmcnt(1)
	v_mfma_f32_32x32x16_bf16 v[16:31], v[34:37], v[116:119], v[16:31]
	v_or_b32_e32 v34, 0x60, v32
	v_bitop3_b32 v34, v34, v33, v42 bitop3:0xde
	v_add_u32_e32 v193, 0, v34
	s_waitcnt lgkmcnt(0)
	v_mfma_f32_32x32x16_bf16 v[0:15], v[38:41], v[116:119], v[0:15]
	ds_read_b128 v[34:37], v193 offset:32768
	ds_read_b128 v[38:41], v193 offset:40960
	s_waitcnt vmcnt(4) lgkmcnt(1)
	v_mfma_f32_32x32x16_bf16 v[16:31], v[34:37], v[112:115], v[16:31]
	v_or_b32_e32 v34, 0x80, v32
	v_bitop3_b32 v34, v34, v33, v42 bitop3:0xde
	v_add_u32_e32 v192, 0, v34
	s_waitcnt lgkmcnt(0)
	v_mfma_f32_32x32x16_bf16 v[0:15], v[38:41], v[112:115], v[0:15]
	ds_read_b128 v[34:37], v192 offset:32768
	ds_read_b128 v[38:41], v192 offset:40960
	s_waitcnt vmcnt(3) lgkmcnt(1)
	v_mfma_f32_32x32x16_bf16 v[16:31], v[34:37], v[108:111], v[16:31]
	v_or_b32_e32 v34, 0xa0, v32
	v_bitop3_b32 v34, v34, v33, v42 bitop3:0xde
	v_add_u32_e32 v191, 0, v34
	s_waitcnt lgkmcnt(0)
	v_mfma_f32_32x32x16_bf16 v[0:15], v[38:41], v[108:111], v[0:15]
	ds_read_b128 v[34:37], v191 offset:32768
	ds_read_b128 v[38:41], v191 offset:40960
	s_waitcnt vmcnt(2) lgkmcnt(1)
	v_mfma_f32_32x32x16_bf16 v[16:31], v[34:37], v[104:107], v[16:31]
	v_or_b32_e32 v34, 0xc0, v32
	v_bitop3_b32 v34, v34, v33, v42 bitop3:0xde
	v_add_u32_e32 v190, 0, v34
	v_or_b32_e32 v32, 0xe0, v32
	v_bitop3_b32 v32, v32, v33, v42 bitop3:0xde
	v_add_u32_e32 v189, 0, v32
	s_waitcnt lgkmcnt(0)
	v_mfma_f32_32x32x16_bf16 v[0:15], v[38:41], v[104:107], v[0:15]
	ds_read_b128 v[34:37], v190 offset:32768
	ds_read_b128 v[38:41], v190 offset:40960
	s_waitcnt vmcnt(1) lgkmcnt(1)
	v_mfma_f32_32x32x16_bf16 v[16:31], v[34:37], v[100:103], v[16:31]
	s_waitcnt lgkmcnt(0)
	v_mfma_f32_32x32x16_bf16 v[0:15], v[38:41], v[100:103], v[0:15]
	ds_read_b128 v[32:35], v189 offset:32768
	ds_read_b128 v[36:39], v189 offset:40960
	s_waitcnt vmcnt(0) lgkmcnt(1)
	v_mfma_f32_32x32x16_bf16 v[16:31], v[32:35], v[96:99], v[16:31]
	s_waitcnt lgkmcnt(0)
	v_mfma_f32_32x32x16_bf16 v[0:15], v[36:39], v[96:99], v[0:15]
	s_nop 9
	v_max_f32_e32 v32, v17, v17
	v_max_f32_e32 v33, v16, v16
	v_max_f32_e32 v32, v33, v32
	v_max_f32_e32 v33, v25, v25
	v_max_f32_e32 v34, v24, v24
	v_max_f32_e32 v33, v34, v33
	v_max3_f32 v32, v32, v18, v19
	v_max_f32_e32 v34, v9, v9
	v_max_f32_e32 v35, v8, v8
	v_max_f32_e32 v34, v35, v34
	v_max3_f32 v35, v0, v1, v2
	v_max3_f32 v34, v34, v10, v11
	v_max3_f32 v33, v33, v26, v27
	v_max3_f32 v35, v35, v3, v4
	v_max3_f32 v34, v34, v12, v13
	v_max3_f32 v32, v32, v20, v21
	v_max3_f32 v33, v33, v28, v29
	v_max3_f32 v35, v35, v5, v6
	v_max3_f32 v34, v34, v14, v15
	v_max3_f32 v32, v32, v22, v23
	v_max3_f32 v33, v33, v30, v31
	v_max3_f32 v34, v35, v7, v34
	v_max3_f32 v32, v32, v33, v34
	v_mov_b32_e32 v33, v32
	s_nop 1
	v_permlane32_swap_b32_e32 v32, v33
	v_max_f32_e32 v33, v33, v33
	v_max_f32_e32 v32, v32, v32
	v_max_f32_e32 v32, v32, v33
	v_add_f32_e32 v33, 0x7149f2ca, v32
	v_max_f32_e32 v32, 0xf149f2ca, v32
	v_cmp_ge_f32_e32 vcc, s31, v33
	v_sub_f32_e32 v33, 0xf149f2ca, v32
	v_mul_f32_e32 v33, 0x3e0293ee, v33
	s_cmp_eq_u64 vcc, exec
	v_exp_f32_e32 v33, v33
	s_cselect_b64 vcc, -1, 0
	v_cndmask_b32_e32 v206, v32, v230, vcc
	s_add_u32 s2, s8, s76
	v_mul_f32_e32 v32, 0xbe0293ee, v206
	s_addc_u32 s3, s9, s77
	v_cndmask_b32_e64 v205, v33, 1.0, vcc
	v_mov_b32_e32 v33, v32
	s_add_u32 s10, s6, s76
	v_fmac_f32_e32 v33, 0x3e0293ee, v31
	s_addc_u32 s11, s7, s77
	v_pk_fma_f32 v[146:147], v[14:15], s[52:53], v[32:33] op_sel_hi:[1,0,0]
	v_pk_fma_f32 v[148:149], v[12:13], s[52:53], v[32:33] op_sel_hi:[1,0,0]
	v_pk_fma_f32 v[150:151], v[10:11], s[52:53], v[32:33] op_sel_hi:[1,0,0]
	v_pk_fma_f32 v[152:153], v[8:9], s[52:53], v[32:33] op_sel_hi:[1,0,0]
	v_pk_fma_f32 v[154:155], v[6:7], s[52:53], v[32:33] op_sel_hi:[1,0,0]
	v_pk_fma_f32 v[156:157], v[4:5], s[52:53], v[32:33] op_sel_hi:[1,0,0]
	v_pk_fma_f32 v[158:159], v[2:3], s[52:53], v[32:33] op_sel_hi:[1,0,0]
	v_pk_fma_f32 v[160:161], v[0:1], s[52:53], v[32:33] op_sel_hi:[1,0,0]
	global_load_dwordx4 v[0:3], v128, s[2:3]
	global_load_dwordx4 v[4:7], v178, s[2:3]
	global_load_dwordx4 v[8:11], v128, s[10:11]
	global_load_dwordx4 v[12:15], v178, s[10:11]
	s_add_u32 s2, s2, s76
	s_addc_u32 s3, s3, s77
	s_add_u32 s10, s10, s76
	s_addc_u32 s11, s11, s77
	global_load_dwordx4 v[130:133], v128, s[2:3]
	global_load_dwordx4 v[134:137], v178, s[2:3]
	global_load_dwordx4 v[138:141], v128, s[10:11]
	global_load_dwordx4 v[142:145], v178, s[10:11]
	v_fmamk_f32 v16, v16, 0x3e0293ee, v32
	v_fmamk_f32 v17, v17, 0x3e0293ee, v32
	v_fmamk_f32 v18, v18, 0x3e0293ee, v32
	v_fmamk_f32 v19, v19, 0x3e0293ee, v32
	v_fmamk_f32 v20, v20, 0x3e0293ee, v32
	v_fmamk_f32 v21, v21, 0x3e0293ee, v32
	v_fmamk_f32 v22, v22, 0x3e0293ee, v32
	v_fmamk_f32 v23, v23, 0x3e0293ee, v32
	v_fmamk_f32 v24, v24, 0x3e0293ee, v32
	v_fmamk_f32 v25, v25, 0x3e0293ee, v32
	v_fmamk_f32 v26, v26, 0x3e0293ee, v32
	v_fmamk_f32 v27, v27, 0x3e0293ee, v32
	v_fmamk_f32 v28, v28, 0x3e0293ee, v32
	v_fmamk_f32 v29, v29, 0x3e0293ee, v32
	v_fmamk_f32 v30, v30, 0x3e0293ee, v32
	v_exp_f32_e32 v176, v16
	v_exp_f32_e32 v211, v17
	v_exp_f32_e32 v163, v18
	v_exp_f32_e32 v177, v19
	v_exp_f32_e32 v164, v20
	v_exp_f32_e32 v175, v21
	v_exp_f32_e32 v165, v22
	v_exp_f32_e32 v174, v23
	v_exp_f32_e32 v166, v24
	v_exp_f32_e32 v173, v25
	v_exp_f32_e32 v167, v26
	v_exp_f32_e32 v172, v27
	v_exp_f32_e32 v168, v28
	v_exp_f32_e32 v171, v29
	v_exp_f32_e32 v169, v30
	v_exp_f32_e32 v170, v33
	s_waitcnt vmcnt(4)
	ds_write_b128 v201, v[0:3] offset:16384
	ds_write_b128 v202, v[4:7] offset:16384
	ds_write_b128 v203, v[8:11] offset:49152
	ds_write_b128 v204, v[12:15] offset:49152
	v_mov_b32_e32 v15, 0
	s_cmp_lt_i32 s19, 3
	s_waitcnt lgkmcnt(0)
	s_barrier
	s_cbranch_scc1 .LBB0_838
	s_add_i32 s20, s17, -4
	s_add_i32 s21, s19, -1
	s_cmp_lg_u32 0, -1
	s_cselect_b32 s2, 0, 0
	s_addk_i32 s2, 0x4000
	s_movk_i32 s3, 0x7c
	v_add_u32_e32 v207, s2, v181
	s_mul_i32 s2, s17, 0x7c
	v_mul_lo_u32 v0, v184, s3
	v_sub_u32_e32 v0, s2, v0
	s_add_i32 s2, 0, 0x14a2c
	v_mov_b32_e32 v187, 0
	v_mov_b32_e32 v179, v129
	v_add_u32_e32 v208, s2, v0
	s_mov_b32 s23, 4
	s_movk_i32 s22, 0xc0
	v_mov_b32_e32 v48, 0
	v_mov_b32_e32 v49, v187
	v_mov_b32_e32 v50, v187
	v_mov_b32_e32 v51, v187
	v_mov_b32_e32 v52, v187
	v_mov_b32_e32 v53, v187
	v_mov_b32_e32 v54, v187
	v_mov_b32_e32 v55, v187
	v_mov_b32_e32 v56, v187
	v_mov_b32_e32 v57, v187
	v_mov_b32_e32 v58, v187
	v_mov_b32_e32 v59, v187
	v_mov_b32_e32 v60, v187
	v_mov_b32_e32 v61, v187
	v_mov_b32_e32 v62, v187
	v_mov_b32_e32 v63, v187
	v_mov_b32_e32 v32, 0
	v_mov_b32_e32 v33, v187
	v_mov_b32_e32 v34, v187
	v_mov_b32_e32 v35, v187
	v_mov_b32_e32 v36, v187
	v_mov_b32_e32 v37, v187
	v_mov_b32_e32 v38, v187
	v_mov_b32_e32 v39, v187
	v_mov_b32_e32 v40, v187
	v_mov_b32_e32 v41, v187
	v_mov_b32_e32 v42, v187
	v_mov_b32_e32 v43, v187
	v_mov_b32_e32 v44, v187
	v_mov_b32_e32 v45, v187
	v_mov_b32_e32 v46, v187
	v_mov_b32_e32 v47, v187
	v_mov_b32_e32 v16, 0
	v_mov_b32_e32 v17, v187
	v_mov_b32_e32 v18, v187
	v_mov_b32_e32 v19, v187
	v_mov_b32_e32 v20, v187
	v_mov_b32_e32 v21, v187
	v_mov_b32_e32 v22, v187
	v_mov_b32_e32 v23, v187
	v_mov_b32_e32 v24, v187
	v_mov_b32_e32 v25, v187
	v_mov_b32_e32 v26, v187
	v_mov_b32_e32 v27, v187
	v_mov_b32_e32 v28, v187
	v_mov_b32_e32 v29, v187
	v_mov_b32_e32 v30, v187
	v_mov_b32_e32 v31, v187
	v_mov_b32_e32 v0, 0
	v_mov_b32_e32 v1, v187
	v_mov_b32_e32 v2, v187
	v_mov_b32_e32 v3, v187
	v_mov_b32_e32 v4, v187
	v_mov_b32_e32 v5, v187
	v_mov_b32_e32 v6, v187
	v_mov_b32_e32 v7, v187
	v_mov_b32_e32 v8, v187
	v_mov_b32_e32 v9, v187
	v_mov_b32_e32 v10, v187
	v_mov_b32_e32 v11, v187
	v_mov_b32_e32 v12, v187
	v_mov_b32_e32 v13, v187
	v_mov_b32_e32 v14, v187
	v_mov_b32_e32 v15, v187
	.p2alignl 3, 3212836864

.LBB0_860:
	s_waitcnt vmcnt(4)
	v_add_u32_e32 v41, 32, v72
	v_and_b32_e32 v36, 63, v71
	v_and_b32_e32 v37, 0xfffff0, v72
	v_lshlrev_b32_e32 v38, 1, v72
	v_and_b32_e32 v42, 0xfffff0, v41
	v_lshlrev_b32_e32 v43, 1, v41
	v_and_or_b32 v37, v38, 8, v37
	v_and_or_b32 v42, v43, 8, v42
	v_lshlrev_b32_e32 v44, 4, v36
	s_and_b64 s[2:3], s[22:23], exec
	v_lshrrev_b32_e32 v38, 1, v72
	v_lshrrev_b32_e32 v37, 1, v37
	v_lshrrev_b32_e32 v39, 5, v74
	v_and_b32_e32 v40, 3, v72
	v_lshrrev_b32_e32 v42, 1, v42
	v_lshlrev_b32_e32 v43, 3, v36
	v_and_b32_e32 v45, 0xc0, v44
	v_lshlrev_b32_e32 v36, 1, v36
	s_cselect_b32 s22, 4, 36
	v_or_b32_e32 v37, v37, v39
	v_and_or_b32 v38, v38, 4, v40
	v_lshlrev_b32_e32 v40, 1, v74
	v_or_b32_e32 v39, v42, v39
	v_and_or_b32 v45, v43, 24, v45
	v_and_b32_e32 v36, 32, v36
	v_and_b32_e32 v43, 0x100, v43
	s_cmp_lg_u32 0, -1
	v_lshlrev_b32_e32 v37, 9, v37
	v_lshlrev_b32_e32 v38, 6, v38
	v_lshlrev_b32_e32 v39, 9, v39
	v_or3_b32 v48, v45, v36, v43
	v_and_b32_e32 v36, 48, v40
	s_cselect_b32 s24, 0, 0
	s_add_i32 s2, 0, 0x15000
	v_or3_b32 v37, v37, v38, v36
	v_or3_b32 v36, v39, v38, v36
	v_lshl_add_u32 v38, v73, 12, s2
	v_add_u32_e32 v204, v38, v44
	s_waitcnt vmcnt(3)
	ds_write_b128 v204, v[24:27]
	s_waitcnt vmcnt(2)
	ds_write_b128 v204, v[20:23] offset:1024
	s_waitcnt vmcnt(1)
	ds_write_b128 v204, v[32:35] offset:2048
	s_waitcnt vmcnt(0)
	ds_write_b128 v204, v[28:31] offset:3072
	v_add_u32_e32 v205, 0, v37
	v_lshrrev_b32_e32 v37, 3, v205
	v_xor_b32_e32 v37, v37, v205
	v_and_b32_e32 v37, 0x100, v37
	v_xor_b32_e32 v205, v205, v37
	v_lshlrev_b32_e32 v37, 3, v37
	v_xor_b32_e32 v205, v205, v37
	ds_write_b128 v205, v[12:15]
	v_lshlrev_b32_e32 v12, 8, v72
	v_and_b32_e32 v13, 0x70, v71
	v_bitop3_b32 v12, v40, v12, v13 bitop3:0xde
	v_add_u32_e32 v206, 0, v36
	v_lshrrev_b32_e32 v36, 3, v206
	v_xor_b32_e32 v36, v36, v206
	v_and_b32_e32 v36, 0x100, v36
	v_xor_b32_e32 v206, v206, v36
	v_lshlrev_b32_e32 v36, 3, v36
	v_xor_b32_e32 v206, v206, v36
	v_add_u32_e32 v207, 0, v12
	ds_write_b128 v206, v[16:19]
	ds_write_b128 v207, v[8:11] offset:32768
	v_lshlrev_b32_e32 v8, 8, v41
	v_bitop3_b32 v8, v40, v8, v13 bitop3:0xde
	v_add_u32_e32 v208, 0, v8
	v_and_b32_e32 v42, 0xffffff80, v96
	ds_write_b128 v208, v[4:7] offset:32768
	v_xor_b32_e32 v4, v96, v71
	s_movk_i32 s2, 0x70
	v_and_or_b32 v49, v4, s2, v42
	s_add_i32 s2, 0, 0x10000
	v_add_u32_e32 v4, s2, v49
	ds_write_b128 v4, v[0:3]
	v_lshlrev_b32_e32 v0, 4, v70
	v_lshlrev_b32_e32 v58, 8, v70
	v_and_b32_e32 v59, 0x70, v0
	v_bitop3_b32 v0, v68, v58, v59 bitop3:0xde
	v_add_u32_e32 v209, 0, v0
	s_waitcnt lgkmcnt(0)
	s_barrier
	ds_read_b128 v[16:19], v209 offset:32768
	ds_read_b128 v[20:23], v209 offset:40960
	s_waitcnt lgkmcnt(1)
	v_mfma_f32_32x32x16_bf16 v[32:47], v[16:19], v[158:161], 0
	v_or_b32_e32 v62, 32, v68
	v_bitop3_b32 v50, v62, v58, v59 bitop3:0xde
	v_add_u32_e32 v211, 0, v50
	ds_read_b128 v[50:53], v211 offset:32768
	ds_read_b128 v[54:57], v211 offset:40960
	v_or_b32_e32 v63, 64, v68
	v_or_b32_e32 v64, 0x60, v68
	v_lshlrev_b32_e32 v65, 7, v70
	s_waitcnt lgkmcnt(2)
	v_mfma_f32_32x32x16_bf16 v[16:31], v[20:23], v[158:161], 0
	s_mov_b32 s72, s73
	s_mov_b32 s74, s73
	s_mov_b32 s75, s73
	s_mov_b32 s76, s73
	s_mov_b32 s77, s73
	s_mov_b32 s78, s73
	s_mov_b32 s79, s73
	s_waitcnt lgkmcnt(1)
	v_mfma_f32_32x32x16_bf16 v[32:47], v[50:53], v[154:157], v[32:47]
	v_bitop3_b32 v50, v63, v58, v59 bitop3:0xde
	v_add_u32_e32 v212, 0, v50
	s_mov_b32 s80, s73
	s_mov_b32 s81, s73
	s_mov_b32 s82, s73
	s_mov_b32 s83, s73
	s_mov_b32 s84, s73
	s_waitcnt lgkmcnt(0)
	v_mfma_f32_32x32x16_bf16 v[16:31], v[54:57], v[154:157], v[16:31]
	ds_read_b128 v[50:53], v212 offset:32768
	ds_read_b128 v[54:57], v212 offset:40960
	s_mov_b32 s85, s73
	s_mov_b32 s86, s73
	s_mov_b32 s87, s73
	v_mov_b64_e32 v[0:1], s[72:73]
	v_mov_b32_e32 v183, v129
	v_mov_b32_e32 v97, v129
	s_waitcnt lgkmcnt(1)
	v_mfma_f32_32x32x16_bf16 v[32:47], v[50:53], v[150:153], v[32:47]
	v_bitop3_b32 v50, v64, v58, v59 bitop3:0xde
	v_add_u32_e32 v213, 0, v50
	v_mov_b64_e32 v[2:3], s[74:75]
	v_mov_b64_e32 v[4:5], s[76:77]
	v_mov_b64_e32 v[6:7], s[78:79]
	v_mov_b64_e32 v[8:9], s[80:81]
	v_mov_b64_e32 v[10:11], s[82:83]
	s_waitcnt lgkmcnt(0)
	v_mfma_f32_32x32x16_bf16 v[16:31], v[54:57], v[150:153], v[16:31]
	ds_read_b128 v[50:53], v213 offset:32768
	ds_read_b128 v[54:57], v213 offset:40960
	v_mov_b64_e32 v[12:13], s[84:85]
	v_mov_b64_e32 v[14:15], s[86:87]
	v_add_u32_e32 v228, 0, v49
	v_add_u32_e32 v201, s24, v48
	v_add_u32_e32 v229, 0x12000, v228
	s_waitcnt lgkmcnt(1)
	v_mfma_f32_32x32x16_bf16 v[32:47], v[50:53], v[146:149], v[32:47]
	v_or_b32_e32 v50, 0x80, v68
	v_bitop3_b32 v50, v50, v58, v59 bitop3:0xde
	v_add_u32_e32 v215, 0, v50
	v_lshl_add_u64 v[184:185], s[58:59], 0, v[96:97]
	v_lshl_add_u64 v[186:187], s[8:9], 0, v[96:97]
	v_mov_b32_e32 v210, 0
	v_readlane_b32 s80, v255, 48
	s_waitcnt lgkmcnt(0)
	v_mfma_f32_32x32x16_bf16 v[16:31], v[54:57], v[146:149], v[16:31]
	ds_read_b128 v[50:53], v215 offset:32768
	ds_read_b128 v[54:57], v215 offset:40960
	s_movk_i32 s84, 0xffe0
	s_waitcnt lgkmcnt(1)
	v_mfma_f32_32x32x16_bf16 v[32:47], v[50:53], v[142:145], v[32:47]
	v_or_b32_e32 v50, 0xa0, v68
	v_bitop3_b32 v50, v50, v58, v59 bitop3:0xde
	v_add_u32_e32 v217, 0, v50
	s_waitcnt lgkmcnt(0)
	v_mfma_f32_32x32x16_bf16 v[16:31], v[54:57], v[142:145], v[16:31]
	ds_read_b128 v[50:53], v217 offset:32768
	ds_read_b128 v[54:57], v217 offset:40960
	s_waitcnt lgkmcnt(1)
	v_mfma_f32_32x32x16_bf16 v[32:47], v[50:53], v[138:141], v[32:47]
	v_or_b32_e32 v50, 0xc0, v68
	v_bitop3_b32 v50, v50, v58, v59 bitop3:0xde
	v_add_u32_e32 v214, 0, v50
	s_waitcnt lgkmcnt(0)
	v_mfma_f32_32x32x16_bf16 v[16:31], v[54:57], v[138:141], v[16:31]
	ds_read_b128 v[50:53], v214 offset:32768
	ds_read_b128 v[54:57], v214 offset:40960
	s_waitcnt lgkmcnt(1)
	v_mfma_f32_32x32x16_bf16 v[32:47], v[50:53], v[134:137], v[32:47]
	v_or_b32_e32 v50, 0xe0, v68
	v_bitop3_b32 v50, v50, v58, v59 bitop3:0xde
	v_add_u32_e32 v216, 0, v50
	s_waitcnt lgkmcnt(0)
	v_mfma_f32_32x32x16_bf16 v[16:31], v[54:57], v[134:137], v[16:31]
	ds_read_b128 v[50:53], v216 offset:32768
	ds_read_b128 v[54:57], v216 offset:40960
	s_waitcnt lgkmcnt(1)
	v_mfma_f32_32x32x16_bf16 v[32:47], v[50:53], v[130:133], v[32:47]
	v_lshlrev_b32_e32 v50, 3, v70
	v_and_b32_e32 v66, 0x70, v50
	v_bitop3_b32 v218, v68, v65, v66 bitop3:0xde
	v_add_u32_e32 v219, s2, v218
	v_bitop3_b32 v220, v62, v65, v66 bitop3:0xde
	v_add_u32_e32 v221, s2, v220
	v_bitop3_b32 v222, v63, v65, v66 bitop3:0xde
	s_waitcnt lgkmcnt(0)
	v_mfma_f32_32x32x16_bf16 v[16:31], v[54:57], v[130:133], v[16:31]
	ds_read_b128 v[50:53], v219
	ds_read_b128 v[54:57], v219 offset:4096
	ds_read_b128 v[58:61], v204
	v_add_u32_e32 v223, s2, v222
	v_bitop3_b32 v224, v64, v65, v66 bitop3:0xde
	v_add_u32_e32 v225, s2, v224
	s_waitcnt lgkmcnt(0)
	v_mfma_f32_32x32x16_bf16 v[32:47], v[50:53], v[58:61], v[32:47]
	v_mfma_f32_32x32x16_bf16 v[16:31], v[54:57], v[58:61], v[16:31]
	ds_read_b128 v[50:53], v221
	ds_read_b128 v[54:57], v221 offset:4096
	ds_read_b128 v[58:61], v204 offset:1024
	s_waitcnt lgkmcnt(0)
	v_mfma_f32_32x32x16_bf16 v[32:47], v[50:53], v[58:61], v[32:47]
	v_mfma_f32_32x32x16_bf16 v[16:31], v[54:57], v[58:61], v[16:31]
	ds_read_b128 v[50:53], v223
	ds_read_b128 v[54:57], v223 offset:4096
	ds_read_b128 v[58:61], v204 offset:2048
	s_waitcnt lgkmcnt(0)
	v_mfma_f32_32x32x16_bf16 v[32:47], v[50:53], v[58:61], v[32:47]
	v_mfma_f32_32x32x16_bf16 v[16:31], v[54:57], v[58:61], v[16:31]
	ds_read_b128 v[50:53], v225
	ds_read_b128 v[54:57], v225 offset:4096
	ds_read_b128 v[58:61], v204 offset:3072
	s_waitcnt lgkmcnt(0)
	v_mfma_f32_32x32x16_bf16 v[32:47], v[50:53], v[58:61], v[32:47]
	v_mfma_f32_32x32x16_bf16 v[16:31], v[54:57], v[58:61], v[16:31]
	s_nop 10
	v_max_f32_e32 v50, v33, v33
	v_max_f32_e32 v51, v32, v32
	v_max_f32_e32 v50, v51, v50
	v_max_f32_e32 v51, v41, v41
	v_max_f32_e32 v52, v40, v40
	v_max_f32_e32 v51, v52, v51
	v_max3_f32 v50, v50, v34, v35
	v_max_f32_e32 v52, v25, v25
	v_max_f32_e32 v53, v24, v24
	v_max_f32_e32 v52, v53, v52
	v_max3_f32 v53, v16, v17, v18
	v_max3_f32 v52, v52, v26, v27
	v_max3_f32 v51, v51, v42, v43
	v_max3_f32 v53, v53, v19, v20
	v_max3_f32 v52, v52, v28, v29
	v_max3_f32 v50, v50, v36, v37
	v_max3_f32 v51, v51, v44, v45
	v_max3_f32 v53, v53, v21, v22
	v_max3_f32 v52, v52, v30, v31
	v_max3_f32 v50, v50, v38, v39
	v_max3_f32 v51, v51, v46, v47
	v_max3_f32 v52, v53, v23, v52
	v_max3_f32 v50, v50, v51, v52
	v_mov_b32_e32 v51, v50
	s_nop 1
	v_permlane32_swap_b32_e32 v50, v51
	v_max_f32_e32 v51, v51, v51
	v_max_f32_e32 v50, v50, v50
	v_max_f32_e32 v50, v50, v51
	v_add_f32_e32 v51, 0x7149f2ca, v50
	v_max_f32_e32 v50, 0xf149f2ca, v50
	v_cmp_ge_f32_e32 vcc, s34, v51
	v_sub_f32_e32 v51, 0xf149f2ca, v50
	v_mul_f32_e32 v51, 0x3dd53b94, v51
	s_cmp_eq_u64 vcc, exec
	v_exp_f32_e32 v51, v51
	s_cselect_b64 vcc, -1, 0
	v_cndmask_b32_e32 v227, v50, v230, vcc
	v_mul_f32_e32 v50, 0xbdd53b94, v227
	v_cndmask_b32_e64 v226, v51, 1.0, vcc
	v_mov_b32_e32 v51, v50
	s_add_u32 s2, s18, s92
	v_fmac_f32_e32 v51, 0x3dd53b94, v47
	s_addc_u32 s3, s19, s93
	v_fmamk_f32 v32, v32, 0x3dd53b94, v50
	v_fmamk_f32 v33, v33, 0x3dd53b94, v50
	v_pk_fma_f32 v[80:81], v[16:17], s[54:55], v[50:51] op_sel_hi:[1,0,0]
	s_add_u32 s74, s16, s92
	v_lshl_add_u64 v[16:17], s[2:3], 0, v[128:129]
	v_fmamk_f32 v34, v34, 0x3dd53b94, v50
	v_fmamk_f32 v35, v35, 0x3dd53b94, v50
	v_pk_fma_f32 v[84:85], v[20:21], s[54:55], v[50:51] op_sel_hi:[1,0,0]
	v_pk_fma_f32 v[82:83], v[18:19], s[54:55], v[50:51] op_sel_hi:[1,0,0]
	v_exp_f32_e32 v64, v32
	v_exp_f32_e32 v65, v33
	s_addc_u32 s75, s17, s93
	global_load_dwordx4 v[16:19], v[16:17], off
	v_lshl_add_u64 v[20:21], s[2:3], 0, v[182:183]
	v_lshl_add_u64 v[32:33], s[96:97], 0, v[96:97]
	v_pk_fma_f32 v[88:89], v[24:25], s[54:55], v[50:51] op_sel_hi:[1,0,0]
	v_pk_fma_f32 v[86:87], v[22:23], s[54:55], v[50:51] op_sel_hi:[1,0,0]
	v_exp_f32_e32 v66, v34
	v_exp_f32_e32 v67, v35
	global_load_dwordx4 v[20:23], v[20:21], off
	v_lshl_add_u64 v[24:25], s[74:75], 0, v[128:129]
	global_load_dwordx4 v[32:35], v[32:33], off
	v_pk_fma_f32 v[92:93], v[28:29], s[54:55], v[50:51] op_sel_hi:[1,0,0]
	v_pk_fma_f32 v[90:91], v[26:27], s[54:55], v[50:51] op_sel_hi:[1,0,0]
	global_load_dwordx4 v[24:27], v[24:25], off
	v_lshl_add_u64 v[28:29], s[74:75], 0, v[182:183]
	v_pk_fma_f32 v[94:95], v[30:31], s[54:55], v[50:51] op_sel_hi:[1,0,0]
	global_load_dwordx4 v[28:31], v[28:29], off
	v_fmamk_f32 v36, v36, 0x3dd53b94, v50
	v_fmamk_f32 v37, v37, 0x3dd53b94, v50
	v_fmamk_f32 v38, v38, 0x3dd53b94, v50
	v_fmamk_f32 v39, v39, 0x3dd53b94, v50
	v_fmamk_f32 v40, v40, 0x3dd53b94, v50
	v_fmamk_f32 v41, v41, 0x3dd53b94, v50
	v_fmamk_f32 v42, v42, 0x3dd53b94, v50
	v_fmamk_f32 v43, v43, 0x3dd53b94, v50
	v_fmamk_f32 v44, v44, 0x3dd53b94, v50
	v_fmamk_f32 v45, v45, 0x3dd53b94, v50
	v_fmamk_f32 v46, v46, 0x3dd53b94, v50
	v_exp_f32_e32 v68, v36
	v_exp_f32_e32 v69, v37
	v_exp_f32_e32 v70, v38
	v_exp_f32_e32 v71, v39
	v_exp_f32_e32 v72, v40
	v_exp_f32_e32 v73, v41
	v_exp_f32_e32 v74, v42
	v_exp_f32_e32 v75, v43
	v_exp_f32_e32 v76, v44
	v_exp_f32_e32 v77, v45
	v_exp_f32_e32 v78, v46
	v_exp_f32_e32 v79, v51
	s_waitcnt vmcnt(0)
	ds_write_b128 v205, v[16:19] offset:16384
	ds_write_b128 v206, v[20:23] offset:16384
	ds_write_b128 v207, v[24:27] offset:49152
	ds_write_b128 v208, v[28:31] offset:49152
	s_addk_i32 s24, 0x4000
	v_lshl_add_u64 v[16:17], s[20:21], 0, v[128:129]
	v_lshl_add_u64 v[18:19], s[20:21], 0, v[182:183]
	ds_write_b128 v229, v[32:35]
	v_add_u32_e32 v203, s24, v48
	v_lshl_add_u64 v[188:189], s[12:13], 0, v[16:17]
	v_lshl_add_u64 v[190:191], s[12:13], 0, v[18:19]
	v_lshl_add_u64 v[192:193], s[14:15], 0, v[16:17]
	v_lshl_add_u64 v[198:199], s[14:15], 0, v[18:19]
	v_mov_b64_e32 v[62:63], v[14:15]
	v_mov_b64_e32 v[46:47], v[14:15]
	v_mov_b64_e32 v[30:31], v[14:15]
	s_add_i32 s23, s22, -1
	s_mov_b32 s20, 2
	v_mov_b64_e32 v[60:61], v[12:13]
	v_mov_b64_e32 v[58:59], v[10:11]
	v_mov_b64_e32 v[56:57], v[8:9]
	v_mov_b64_e32 v[54:55], v[6:7]
	v_mov_b64_e32 v[52:53], v[4:5]
	v_mov_b64_e32 v[50:51], v[2:3]
	v_mov_b64_e32 v[48:49], v[0:1]
	v_mov_b64_e32 v[44:45], v[12:13]
	v_mov_b64_e32 v[42:43], v[10:11]
	v_mov_b64_e32 v[40:41], v[8:9]
	v_mov_b64_e32 v[38:39], v[6:7]
	v_mov_b64_e32 v[36:37], v[4:5]
	v_mov_b64_e32 v[34:35], v[2:3]
	v_mov_b64_e32 v[32:33], v[0:1]
	v_mov_b64_e32 v[28:29], v[12:13]
	v_mov_b64_e32 v[26:27], v[10:11]
	v_mov_b64_e32 v[24:25], v[8:9]
	v_mov_b64_e32 v[22:23], v[6:7]
	v_mov_b64_e32 v[20:21], v[4:5]
	v_mov_b64_e32 v[18:19], v[2:3]
	v_mov_b64_e32 v[16:17], v[0:1]
	v_readlane_b32 s21, v252, 17
	s_waitcnt lgkmcnt(0)
	s_barrier
	.p2alignl 3, 3212836864

.LBB0_967:
	s_and_b64 s[2:3], s[86:87], exec
	s_cselect_b32 s2, s79, s38
	s_lshr_b32 s2, s2, 12
	s_and_b32 s72, s2, 0x80000
	s_and_b64 s[2:3], s[86:87], exec
	s_cselect_b32 s15, s83, s19
	s_cselect_b32 s17, s82, s18
	s_cselect_b32 s67, s23, s85
	s_cselect_b32 s3, s22, s84
	s_cmp_lt_i32 s38, 0
	s_cselect_b64 s[96:97], -1, 0
	s_add_u32 s24, s18, 0x80
	s_addc_u32 s25, s19, 0
	v_lshl_add_u64 v[0:1], s[24:25], 0, v[202:203]
	v_lshl_add_u64 v[206:207], v[0:1], 0, s[20:21]
	v_lshl_add_u64 v[0:1], s[24:25], 0, v[204:205]
	v_mov_b32_e32 v128, v129
	v_lshl_add_u64 v[208:209], v[0:1], 0, s[20:21]
	s_add_u32 s2, s84, 0x100
	s_waitcnt vmcnt(0)
	v_mov_b32_e32 v130, v129
	v_mov_b32_e32 v131, v129
	v_mov_b32_e32 v64, 0
	v_mov_b64_e32 v[0:1], v[128:129]
	v_mov_b64_e32 v[4:5], v[128:129]
	v_mov_b64_e32 v[16:17], v[128:129]
	v_mov_b64_e32 v[20:21], v[128:129]
	v_mov_b64_e32 v[32:33], v[128:129]
	v_mov_b64_e32 v[36:37], v[128:129]
	v_mov_b64_e32 v[48:49], v[128:129]
	v_mov_b64_e32 v[52:53], v[128:129]
	v_mov_b64_e32 v[8:9], v[128:129]
	v_mov_b64_e32 v[12:13], v[128:129]
	v_mov_b64_e32 v[24:25], v[128:129]
	v_mov_b64_e32 v[28:29], v[128:129]
	v_mov_b64_e32 v[40:41], v[128:129]
	v_mov_b64_e32 v[44:45], v[128:129]
	v_mov_b64_e32 v[56:57], v[128:129]
	v_mov_b64_e32 v[60:61], v[128:129]
	s_addc_u32 s29, s85, 0
	s_mov_b32 s30, -2
	v_mov_b64_e32 v[2:3], v[130:131]
	v_mov_b64_e32 v[6:7], v[130:131]
	v_mov_b64_e32 v[18:19], v[130:131]
	v_mov_b64_e32 v[22:23], v[130:131]
	v_mov_b64_e32 v[34:35], v[130:131]
	v_mov_b64_e32 v[38:39], v[130:131]
	v_mov_b64_e32 v[50:51], v[130:131]
	v_mov_b64_e32 v[54:55], v[130:131]
	v_mov_b64_e32 v[10:11], v[130:131]
	v_mov_b64_e32 v[14:15], v[130:131]
	v_mov_b64_e32 v[26:27], v[130:131]
	v_mov_b64_e32 v[30:31], v[130:131]
	v_mov_b64_e32 v[42:43], v[130:131]
	v_mov_b64_e32 v[46:47], v[130:131]
	v_mov_b64_e32 v[58:59], v[130:131]
	v_mov_b64_e32 v[62:63], v[130:131]
	v_mov_b32_e32 v65, v64
	v_mov_b32_e32 v66, v64
	v_mov_b32_e32 v67, v64
	v_mov_b32_e32 v68, v64
	v_mov_b32_e32 v69, v64
	v_mov_b32_e32 v70, v64
	v_mov_b32_e32 v71, v64
	v_mov_b32_e32 v80, v64
	v_mov_b32_e32 v81, v64
	v_mov_b32_e32 v82, v64
	v_mov_b32_e32 v83, v64
	v_mov_b32_e32 v84, v64
	v_mov_b32_e32 v85, v64
	v_mov_b32_e32 v86, v64
	v_mov_b32_e32 v87, v64
	v_mov_b32_e32 v96, v64
	v_mov_b32_e32 v97, v64
	v_mov_b32_e32 v98, v64
	v_mov_b32_e32 v99, v64
	v_mov_b32_e32 v100, v64
	v_mov_b32_e32 v101, v64
	v_mov_b32_e32 v102, v64
	v_mov_b32_e32 v103, v64
	v_mov_b32_e32 v124, v64
	v_mov_b32_e32 v125, v64
	v_mov_b32_e32 v126, v64
	v_mov_b32_e32 v127, v64
	v_mov_b32_e32 v134, v64
	v_mov_b32_e32 v135, v64
	v_mov_b32_e32 v136, v64
	v_mov_b32_e32 v137, v64
	v_mov_b32_e32 v72, v64
	v_mov_b32_e32 v73, v64
	v_mov_b32_e32 v74, v64
	v_mov_b32_e32 v75, v64
	v_mov_b32_e32 v76, v64
	v_mov_b32_e32 v77, v64
	v_mov_b32_e32 v78, v64
	v_mov_b32_e32 v79, v64
	v_mov_b32_e32 v88, v64
	v_mov_b32_e32 v89, v64
	v_mov_b32_e32 v90, v64
	v_mov_b32_e32 v91, v64
	v_mov_b32_e32 v92, v64
	v_mov_b32_e32 v93, v64
	v_mov_b32_e32 v94, v64
	v_mov_b32_e32 v95, v64
	v_mov_b32_e32 v112, v64
	v_mov_b32_e32 v113, v64
	v_mov_b32_e32 v114, v64
	v_mov_b32_e32 v115, v64
	v_mov_b32_e32 v120, v64
	v_mov_b32_e32 v121, v64
	v_mov_b32_e32 v122, v64
	v_mov_b32_e32 v123, v64
	v_mov_b32_e32 v138, v64
	v_mov_b32_e32 v139, v64
	v_mov_b32_e32 v140, v64
	v_mov_b32_e32 v141, v64
	v_mov_b32_e32 v142, v64
	v_mov_b32_e32 v143, v64
	v_mov_b32_e32 v144, v64
	v_mov_b32_e32 v145, v64
	s_branch .LBB0_969
	.p2alignl 3, 3212836864

.LBB0_1398:
	v_mov_b32_e32 v128, v129
	s_cmp_lt_i32 s25, 0
	v_mov_b32_e32 v213, v129
	v_mov_b32_e32 v215, v129
	v_lshl_add_u64 v[220:221], v[2:3], 0, s[46:47]
	v_mov_b32_e32 v130, v129
	v_mov_b32_e32 v131, v129
	v_mov_b32_e32 v64, 0
	v_mov_b64_e32 v[0:1], v[128:129]
	v_mov_b64_e32 v[4:5], v[128:129]
	v_mov_b64_e32 v[16:17], v[128:129]
	v_mov_b64_e32 v[20:21], v[128:129]
	v_mov_b64_e32 v[32:33], v[128:129]
	v_mov_b64_e32 v[36:37], v[128:129]
	v_mov_b64_e32 v[48:49], v[128:129]
	v_mov_b64_e32 v[52:53], v[128:129]
	v_mov_b64_e32 v[8:9], v[128:129]
	v_mov_b64_e32 v[12:13], v[128:129]
	v_mov_b64_e32 v[24:25], v[128:129]
	v_mov_b64_e32 v[28:29], v[128:129]
	v_mov_b64_e32 v[40:41], v[128:129]
	v_mov_b64_e32 v[44:45], v[128:129]
	v_mov_b64_e32 v[56:57], v[128:129]
	v_mov_b64_e32 v[60:61], v[128:129]
	s_cselect_b64 s[20:21], -1, 0
	v_lshl_add_u64 v[216:217], s[14:15], 0, v[214:215]
	v_lshl_add_u64 v[218:219], s[14:15], 0, v[212:213]
	s_mov_b32 s24, -2
	s_mov_b64 s[74:75], 0
	v_mov_b64_e32 v[2:3], v[130:131]
	v_mov_b64_e32 v[6:7], v[130:131]
	v_mov_b64_e32 v[18:19], v[130:131]
	v_mov_b64_e32 v[22:23], v[130:131]
	v_mov_b64_e32 v[34:35], v[130:131]
	v_mov_b64_e32 v[38:39], v[130:131]
	v_mov_b64_e32 v[50:51], v[130:131]
	v_mov_b64_e32 v[54:55], v[130:131]
	v_mov_b64_e32 v[10:11], v[130:131]
	v_mov_b64_e32 v[14:15], v[130:131]
	v_mov_b64_e32 v[26:27], v[130:131]
	v_mov_b64_e32 v[30:31], v[130:131]
	v_mov_b64_e32 v[42:43], v[130:131]
	v_mov_b64_e32 v[46:47], v[130:131]
	v_mov_b64_e32 v[58:59], v[130:131]
	v_mov_b64_e32 v[62:63], v[130:131]
	v_mov_b32_e32 v65, v64
	v_mov_b32_e32 v66, v64
	v_mov_b32_e32 v67, v64
	v_mov_b32_e32 v68, v64
	v_mov_b32_e32 v69, v64
	v_mov_b32_e32 v70, v64
	v_mov_b32_e32 v71, v64
	v_mov_b32_e32 v80, v64
	v_mov_b32_e32 v81, v64
	v_mov_b32_e32 v82, v64
	v_mov_b32_e32 v83, v64
	v_mov_b32_e32 v84, v64
	v_mov_b32_e32 v85, v64
	v_mov_b32_e32 v86, v64
	v_mov_b32_e32 v87, v64
	v_mov_b32_e32 v96, v64
	v_mov_b32_e32 v97, v64
	v_mov_b32_e32 v98, v64
	v_mov_b32_e32 v99, v64
	v_mov_b32_e32 v100, v64
	v_mov_b32_e32 v101, v64
	v_mov_b32_e32 v102, v64
	v_mov_b32_e32 v103, v64
	v_mov_b32_e32 v112, v64
	v_mov_b32_e32 v113, v64
	v_mov_b32_e32 v114, v64
	v_mov_b32_e32 v115, v64
	v_mov_b32_e32 v116, v64
	v_mov_b32_e32 v117, v64
	v_mov_b32_e32 v118, v64
	v_mov_b32_e32 v119, v64
	v_mov_b32_e32 v72, v64
	v_mov_b32_e32 v73, v64
	v_mov_b32_e32 v74, v64
	v_mov_b32_e32 v75, v64
	v_mov_b32_e32 v76, v64
	v_mov_b32_e32 v77, v64
	v_mov_b32_e32 v78, v64
	v_mov_b32_e32 v79, v64
	v_mov_b32_e32 v88, v64
	v_mov_b32_e32 v89, v64
	v_mov_b32_e32 v90, v64
	v_mov_b32_e32 v91, v64
	v_mov_b32_e32 v92, v64
	v_mov_b32_e32 v93, v64
	v_mov_b32_e32 v94, v64
	v_mov_b32_e32 v95, v64
	v_mov_b32_e32 v104, v64
	v_mov_b32_e32 v105, v64
	v_mov_b32_e32 v106, v64
	v_mov_b32_e32 v107, v64
	v_mov_b32_e32 v108, v64
	v_mov_b32_e32 v109, v64
	v_mov_b32_e32 v110, v64
	v_mov_b32_e32 v111, v64
	v_mov_b32_e32 v120, v64
	v_mov_b32_e32 v121, v64
	v_mov_b32_e32 v122, v64
	v_mov_b32_e32 v123, v64
	v_mov_b32_e32 v124, v64
	v_mov_b32_e32 v125, v64
	v_mov_b32_e32 v126, v64
	v_mov_b32_e32 v127, v64
	s_branch .LBB0_1400
	.p2alignl 3, 3212836864

.LBB0_1441:
	s_lshl_b32 s2, s18, 3
	s_ashr_i32 s3, s2, 31
	s_lshl_b64 s[2:3], s[2:3], 2
	s_add_u32 s20, s27, s2
	v_mov_b32_e32 v0, 0
	s_addc_u32 s21, s28, s3
	s_mov_b32 s19, 0
	v_mov_b32_e32 v1, v0
	v_mov_b32_e32 v2, v0
	v_mov_b32_e32 v3, v0
	v_mov_b32_e32 v4, v0
	v_mov_b32_e32 v5, v0
	v_mov_b32_e32 v6, v0
	v_mov_b32_e32 v7, v0
	v_mov_b32_e32 v12, v0
	v_mov_b32_e32 v13, v0
	v_mov_b32_e32 v14, v0
	v_mov_b32_e32 v15, v0
	v_mov_b32_e32 v20, v0
	v_mov_b32_e32 v21, v0
	v_mov_b32_e32 v22, v0
	v_mov_b32_e32 v23, v0
	v_mov_b32_e32 v28, v0
	v_mov_b32_e32 v29, v0
	v_mov_b32_e32 v30, v0
	v_mov_b32_e32 v31, v0
	v_mov_b32_e32 v36, v0
	v_mov_b32_e32 v37, v0
	v_mov_b32_e32 v38, v0
	v_mov_b32_e32 v39, v0
	v_mov_b32_e32 v44, v0
	v_mov_b32_e32 v45, v0
	v_mov_b32_e32 v46, v0
	v_mov_b32_e32 v47, v0
	v_mov_b32_e32 v52, v0
	v_mov_b32_e32 v53, v0
	v_mov_b32_e32 v54, v0
	v_mov_b32_e32 v55, v0
	v_mov_b32_e32 v8, v0
	v_mov_b32_e32 v9, v0
	v_mov_b32_e32 v10, v0
	v_mov_b32_e32 v11, v0
	v_mov_b32_e32 v16, v0
	v_mov_b32_e32 v17, v0
	v_mov_b32_e32 v18, v0
	v_mov_b32_e32 v19, v0
	v_mov_b32_e32 v24, v0
	v_mov_b32_e32 v25, v0
	v_mov_b32_e32 v26, v0
	v_mov_b32_e32 v27, v0
	v_mov_b32_e32 v32, v0
	v_mov_b32_e32 v33, v0
	v_mov_b32_e32 v34, v0
	v_mov_b32_e32 v35, v0
	v_mov_b32_e32 v40, v0
	v_mov_b32_e32 v41, v0
	v_mov_b32_e32 v42, v0
	v_mov_b32_e32 v43, v0
	v_mov_b32_e32 v48, v0
	v_mov_b32_e32 v49, v0
	v_mov_b32_e32 v50, v0
	v_mov_b32_e32 v51, v0
	v_mov_b32_e32 v56, v0
	v_mov_b32_e32 v57, v0
	v_mov_b32_e32 v58, v0
	v_mov_b32_e32 v59, v0
	v_mov_b32_e32 v60, v0
	v_mov_b32_e32 v61, v0
	v_mov_b32_e32 v62, v0
	v_mov_b32_e32 v63, v0
	v_mov_b32_e32 v64, v0
	v_mov_b32_e32 v65, v0
	v_mov_b32_e32 v66, v0
	v_mov_b32_e32 v67, v0
	v_mov_b32_e32 v68, v0
	v_mov_b32_e32 v69, v0
	v_mov_b32_e32 v70, v0
	v_mov_b32_e32 v71, v0
	v_mov_b32_e32 v76, v0
	v_mov_b32_e32 v77, v0
	v_mov_b32_e32 v78, v0
	v_mov_b32_e32 v79, v0
	v_mov_b32_e32 v84, v0
	v_mov_b32_e32 v85, v0
	v_mov_b32_e32 v86, v0
	v_mov_b32_e32 v87, v0
	v_mov_b32_e32 v92, v0
	v_mov_b32_e32 v93, v0
	v_mov_b32_e32 v94, v0
	v_mov_b32_e32 v95, v0
	v_mov_b32_e32 v100, v0
	v_mov_b32_e32 v101, v0
	v_mov_b32_e32 v102, v0
	v_mov_b32_e32 v103, v0
	v_mov_b32_e32 v108, v0
	v_mov_b32_e32 v109, v0
	v_mov_b32_e32 v110, v0
	v_mov_b32_e32 v111, v0
	v_mov_b32_e32 v116, v0
	v_mov_b32_e32 v117, v0
	v_mov_b32_e32 v118, v0
	v_mov_b32_e32 v119, v0
	v_mov_b32_e32 v72, v0
	v_mov_b32_e32 v73, v0
	v_mov_b32_e32 v74, v0
	v_mov_b32_e32 v75, v0
	v_mov_b32_e32 v80, v0
	v_mov_b32_e32 v81, v0
	v_mov_b32_e32 v82, v0
	v_mov_b32_e32 v83, v0
	v_mov_b32_e32 v88, v0
	v_mov_b32_e32 v89, v0
	v_mov_b32_e32 v90, v0
	v_mov_b32_e32 v91, v0
	v_mov_b32_e32 v96, v0
	v_mov_b32_e32 v97, v0
	v_mov_b32_e32 v98, v0
	v_mov_b32_e32 v99, v0
	v_mov_b32_e32 v104, v0
	v_mov_b32_e32 v105, v0
	v_mov_b32_e32 v106, v0
	v_mov_b32_e32 v107, v0
	v_mov_b32_e32 v112, v0
	v_mov_b32_e32 v113, v0
	v_mov_b32_e32 v114, v0
	v_mov_b32_e32 v115, v0
	v_mov_b32_e32 v120, v0
	v_mov_b32_e32 v121, v0
	v_mov_b32_e32 v122, v0
	v_mov_b32_e32 v123, v0
	v_mov_b32_e32 v124, v0
	v_mov_b32_e32 v125, v0
	v_mov_b32_e32 v126, v0
	v_mov_b32_e32 v127, v0
	s_branch .LBB0_1444
	.p2alignl 3, 3212836864
